# branch-merge epilogue: attention-gate rows of row groups 1-7 loaded together at the epilogue start (dead fragment registers) instead of group by group
# baseline (speedup 1.0000x reference)
; #define GAS __attribute__((address_space(1)))
; #define LAS __attribute__((address_space(3)))
;     __device__ __forceinline__ bool operator()(f32x4 (&acc)[2][2][4][2], const Unit& u, int wr, int wc, int fr, int fq, LAS unsigned char* scr) const {
;         const int lane = fq * 16 + fr, rowb = u.row0 + wr * 64, colb = u.col0 + wc * 64;
;         const int lr = lane >> 3, lch = lane & 7;
;         const int wo = lr * 128 + ((lch ^ (lr & 7)) * 16);
;         const bool seg0 = (u.aux == 0);
; #pragma unroll
;         for (int ai = 0; ai < 2; ++ai)
; #pragma unroll
;             for (int m = 0; m < 4; ++m) { const size_t rg = (size_t)(rowb + ai * 128 + m * 16);
;                 const GAS bf16_t* gpa = H + HOFF(C_GA + colb, rg + lr) + lch * 8; const GAS bf16_t* gph = H + HOFF(C_GH + colb, rg + lr) + lch * 8;
;                 const u32x4 ga0 = *(const GAS u32x4*)gpa, ga1 = *(const GAS u32x4*)(gpa + 8 * 128);
;                 u32x4 gh0 = ga0, gh1 = ga1; if (seg0) { gh0 = *(const GAS u32x4*)gph; gh1 = *(const GAS u32x4*)(gph + 8 * 128); }
;                 *(LAS u32x4*)(scr + wo) = ga0; *(LAS u32x4*)(scr + wo + 1024) = ga1;
;                 u32x4 gaf[2], ghf[2];
; #pragma unroll
;                 for (int bj = 0; bj < 2; ++bj) gaf[bj] = *(const LAS u32x4*)(scr + fr * 128 + (((bj * 4 + fq) ^ (fr & 7)) * 16));
.LBB0_1050:
	s_add_i32 s34, s20, s63
	s_add_i32 s28, s33, s72
	s_cmp_eq_u32 s37, 0
	s_cselect_b64 s[6:7], -1, 0
	s_cmp_lg_u32 s37, 0
	s_cselect_b64 s[38:39], -1, 0
	s_add_i32 s8, s28, 0x2a00
	s_add_i32 s29, s28, 0x2200
	s_ashr_i32 s8, s8, 7
	s_ashr_i32 s30, s29, 7
	s_ashr_i32 s9, s8, 31
	s_ashr_i32 s31, s30, 31
	s_and_b32 s20, s28, 0x7f
	s_lshl_b64 s[8:9], s[8:9], 22
	s_lshl_b64 s[30:31], s[30:31], 22
	s_ashr_i32 s35, s34, 31
	v_lshl_add_u64 v[130:131], s[34:35], 0, v[160:161]
	s_add_u32 s36, s61, s8
	s_addc_u32 s37, s62, s9
	v_lshlrev_b64 v[138:139], 8, v[130:131]
	v_lshl_add_u64 v[130:131], s[36:37], 0, v[138:139]
	s_lshl_b32 s20, s20, 1
	v_lshl_add_u64 v[130:131], v[130:131], 0, s[20:21]
	v_mov_b32_e32 v171, v159
	v_lshl_add_u64 v[134:135], v[130:131], 0, v[170:171]
	s_mov_b64 s[98:99], 0x1000
	s_mov_b64 s[100:101], 0x8000
	v_lshl_add_u64 v[140:141], v[134:135], 0, s[98:99]
	global_load_dwordx4 v[190:193], v[140:141], off
	global_load_dwordx4 v[194:197], v[140:141], off offset:2048
	v_lshl_add_u64 v[140:141], v[140:141], 0, s[98:99]
	global_load_dwordx4 v[198:201], v[140:141], off
	global_load_dwordx4 v[202:205], v[140:141], off offset:2048
	v_lshl_add_u64 v[140:141], v[140:141], 0, s[98:99]
	global_load_dwordx4 v[206:209], v[140:141], off
	global_load_dwordx4 v[210:213], v[140:141], off offset:2048
	v_lshl_add_u64 v[140:141], v[134:135], 0, s[100:101]
	global_load_dwordx4 v[214:217], v[140:141], off
	global_load_dwordx4 v[218:221], v[140:141], off offset:2048
	v_lshl_add_u64 v[140:141], v[140:141], 0, s[98:99]
	global_load_dwordx4 v[222:225], v[140:141], off
	global_load_dwordx4 v[226:229], v[140:141], off offset:2048
	v_lshl_add_u64 v[140:141], v[140:141], 0, s[98:99]
	global_load_dwordx4 v[230:233], v[140:141], off
	global_load_dwordx4 v[234:237], v[140:141], off offset:2048
	v_lshl_add_u64 v[140:141], v[140:141], 0, s[98:99]
	global_load_dwordx4 v[238:241], v[140:141], off
	global_load_dwordx4 v[242:245], v[140:141], off offset:2048
	global_load_dwordx4 v[130:133], v[134:135], off offset:2048
	s_nop 0
	global_load_dwordx4 v[134:137], v[134:135], off
	s_and_b64 vcc, exec, s[38:39]
	s_waitcnt vmcnt(0)
	v_mov_b64_e32 v[148:149], v[132:133]
	v_mov_b64_e32 v[152:153], v[136:137]
	v_mov_b64_e32 v[146:147], v[130:131]
	v_mov_b64_e32 v[150:151], v[134:135]
	s_cbranch_vccnz .LBB0_1052
	s_add_u32 s8, s61, s30
	s_addc_u32 s9, s62, s31
	v_lshl_add_u64 v[138:139], s[8:9], 0, v[138:139]
	v_lshl_add_u64 v[138:139], v[138:139], 0, s[20:21]
	v_lshl_add_u64 v[138:139], v[138:139], 0, v[170:171]
	global_load_dwordx4 v[150:153], v[138:139], off
	global_load_dwordx4 v[146:149], v[138:139], off offset:2048

; #define GAS __attribute__((address_space(1)))
;     __device__ __forceinline__ bool operator()(f32x4 (&acc)[2][2][4][2], const Unit& u, int wr, int wc, int fr, int fq, LAS unsigned char* scr) const {
;     ...
;             for (int m = 0; m < 4; ++m) { const size_t rg = (size_t)(rowb + ai * 128 + m * 16);
;                 const GAS bf16_t* gpa = H + HOFF(C_GA + colb, rg + lr) + lch * 8; const GAS bf16_t* gph = H + HOFF(C_GH + colb, rg + lr) + lch * 8;
;                 const u32x4 ga0 = *(const GAS u32x4*)gpa, ga1 = *(const GAS u32x4*)(gpa + 8 * 128);
;                 u32x4 gh0 = ga0, gh1 = ga1; if (seg0) { gh0 = *(const GAS u32x4*)gph; gh1 = *(const GAS u32x4*)(gph + 8 * 128); }
.LBB0_1062:
	s_add_i32 s38, s34, 16
	s_ashr_i32 s39, s38, 31
	v_lshl_add_u64 v[138:139], s[38:39], 0, v[160:161]
	v_lshlrev_b64 v[180:181], 8, v[138:139]
	v_lshl_add_u64 v[138:139], s[36:37], 0, v[180:181]
	v_lshl_add_u64 v[138:139], v[138:139], 0, s[20:21]
	v_mov_b32_e32 v171, v159
	v_lshl_add_u64 v[142:143], v[138:139], 0, v[170:171]
	v_mov_b64_e32 v[138:139], v[194:195]
	v_mov_b64_e32 v[140:141], v[196:197]
	s_nop 0
	v_mov_b64_e32 v[142:143], v[190:191]
	v_mov_b64_e32 v[144:145], v[192:193]
	s_and_b64 vcc, exec, s[8:9]
	v_mov_b64_e32 v[148:149], v[140:141]
	v_mov_b64_e32 v[152:153], v[144:145]
	v_mov_b64_e32 v[146:147], v[138:139]
	v_mov_b64_e32 v[150:151], v[142:143]
	s_cbranch_vccnz .LBB0_1064
	s_add_u32 s40, s61, s30
	s_addc_u32 s41, s62, s31
	v_lshl_add_u64 v[146:147], s[40:41], 0, v[180:181]
	v_lshl_add_u64 v[146:147], v[146:147], 0, s[20:21]
	v_lshl_add_u64 v[146:147], v[146:147], 0, v[170:171]
	global_load_dwordx4 v[150:153], v[146:147], off
	s_nop 0
	global_load_dwordx4 v[146:149], v[146:147], off offset:2048

; #define GAS __attribute__((address_space(1)))
;     __device__ __forceinline__ bool operator()(f32x4 (&acc)[2][2][4][2], const Unit& u, int wr, int wc, int fr, int fq, LAS unsigned char* scr) const {
;     ...
;             for (int m = 0; m < 4; ++m) { const size_t rg = (size_t)(rowb + ai * 128 + m * 16);
;                 const GAS bf16_t* gpa = H + HOFF(C_GA + colb, rg + lr) + lch * 8; const GAS bf16_t* gph = H + HOFF(C_GH + colb, rg + lr) + lch * 8;
;                 const u32x4 ga0 = *(const GAS u32x4*)gpa, ga1 = *(const GAS u32x4*)(gpa + 8 * 128);
;                 u32x4 gh0 = ga0, gh1 = ga1; if (seg0) { gh0 = *(const GAS u32x4*)gph; gh1 = *(const GAS u32x4*)(gph + 8 * 128); }
.LBB0_1074:
	s_add_i32 s38, s34, 32
	s_ashr_i32 s39, s38, 31
	v_lshl_add_u64 v[138:139], s[38:39], 0, v[160:161]
	v_lshlrev_b64 v[180:181], 8, v[138:139]
	v_lshl_add_u64 v[138:139], s[36:37], 0, v[180:181]
	v_lshl_add_u64 v[138:139], v[138:139], 0, s[20:21]
	v_mov_b32_e32 v171, v159
	v_lshl_add_u64 v[142:143], v[138:139], 0, v[170:171]
	v_mov_b64_e32 v[138:139], v[202:203]
	v_mov_b64_e32 v[140:141], v[204:205]
	s_nop 0
	v_mov_b64_e32 v[142:143], v[198:199]
	v_mov_b64_e32 v[144:145], v[200:201]
	s_and_b64 vcc, exec, s[8:9]
	v_mov_b64_e32 v[148:149], v[140:141]
	v_mov_b64_e32 v[152:153], v[144:145]
	v_mov_b64_e32 v[146:147], v[138:139]
	v_mov_b64_e32 v[150:151], v[142:143]
	s_cbranch_vccnz .LBB0_1076
	s_add_u32 s40, s61, s30
	s_addc_u32 s41, s62, s31
	v_lshl_add_u64 v[146:147], s[40:41], 0, v[180:181]
	v_lshl_add_u64 v[146:147], v[146:147], 0, s[20:21]
	v_lshl_add_u64 v[146:147], v[146:147], 0, v[170:171]
	global_load_dwordx4 v[150:153], v[146:147], off
	s_nop 0
	global_load_dwordx4 v[146:149], v[146:147], off offset:2048

; #define GAS __attribute__((address_space(1)))
;     __device__ __forceinline__ bool operator()(f32x4 (&acc)[2][2][4][2], const Unit& u, int wr, int wc, int fr, int fq, LAS unsigned char* scr) const {
;     ...
;             for (int m = 0; m < 4; ++m) { const size_t rg = (size_t)(rowb + ai * 128 + m * 16);
;                 const GAS bf16_t* gpa = H + HOFF(C_GA + colb, rg + lr) + lch * 8; const GAS bf16_t* gph = H + HOFF(C_GH + colb, rg + lr) + lch * 8;
;                 const u32x4 ga0 = *(const GAS u32x4*)gpa, ga1 = *(const GAS u32x4*)(gpa + 8 * 128);
;                 u32x4 gh0 = ga0, gh1 = ga1; if (seg0) { gh0 = *(const GAS u32x4*)gph; gh1 = *(const GAS u32x4*)(gph + 8 * 128); }
.LBB0_1086:
	s_add_i32 s38, s34, 48
	s_ashr_i32 s39, s38, 31
	v_lshl_add_u64 v[138:139], s[38:39], 0, v[160:161]
	v_lshlrev_b64 v[180:181], 8, v[138:139]
	v_lshl_add_u64 v[138:139], s[36:37], 0, v[180:181]
	v_lshl_add_u64 v[138:139], v[138:139], 0, s[20:21]
	v_mov_b32_e32 v171, v159
	v_lshl_add_u64 v[142:143], v[138:139], 0, v[170:171]
	v_mov_b64_e32 v[138:139], v[210:211]
	v_mov_b64_e32 v[140:141], v[212:213]
	s_nop 0
	v_mov_b64_e32 v[142:143], v[206:207]
	v_mov_b64_e32 v[144:145], v[208:209]
	s_and_b64 vcc, exec, s[8:9]
	v_mov_b64_e32 v[148:149], v[140:141]
	v_mov_b64_e32 v[152:153], v[144:145]
	v_mov_b64_e32 v[146:147], v[138:139]
	v_mov_b64_e32 v[150:151], v[142:143]
	s_cbranch_vccnz .LBB0_1088
	s_add_u32 s40, s61, s30
	s_addc_u32 s41, s62, s31
	v_lshl_add_u64 v[146:147], s[40:41], 0, v[180:181]
	v_lshl_add_u64 v[146:147], v[146:147], 0, s[20:21]
	v_lshl_add_u64 v[146:147], v[146:147], 0, v[170:171]
	global_load_dwordx4 v[150:153], v[146:147], off
	s_nop 0
	global_load_dwordx4 v[146:149], v[146:147], off offset:2048

; #define GAS __attribute__((address_space(1)))
;     __device__ __forceinline__ bool operator()(f32x4 (&acc)[2][2][4][2], const Unit& u, int wr, int wc, int fr, int fq, LAS unsigned char* scr) const {
;     ...
;             for (int m = 0; m < 4; ++m) { const size_t rg = (size_t)(rowb + ai * 128 + m * 16);
;                 const GAS bf16_t* gpa = H + HOFF(C_GA + colb, rg + lr) + lch * 8; const GAS bf16_t* gph = H + HOFF(C_GH + colb, rg + lr) + lch * 8;
;                 const u32x4 ga0 = *(const GAS u32x4*)gpa, ga1 = *(const GAS u32x4*)(gpa + 8 * 128);
;                 u32x4 gh0 = ga0, gh1 = ga1; if (seg0) { gh0 = *(const GAS u32x4*)gph; gh1 = *(const GAS u32x4*)(gph + 8 * 128); }
.LBB0_1098:
	s_add_i32 s38, s34, 0x80
	s_ashr_i32 s39, s38, 31
	v_lshl_add_u64 v[138:139], s[38:39], 0, v[160:161]
	v_lshlrev_b64 v[180:181], 8, v[138:139]
	v_lshl_add_u64 v[138:139], s[36:37], 0, v[180:181]
	v_lshl_add_u64 v[138:139], v[138:139], 0, s[20:21]
	v_mov_b32_e32 v171, v159
	v_lshl_add_u64 v[142:143], v[138:139], 0, v[170:171]
	v_mov_b64_e32 v[138:139], v[218:219]
	v_mov_b64_e32 v[140:141], v[220:221]
	s_nop 0
	v_mov_b64_e32 v[142:143], v[214:215]
	v_mov_b64_e32 v[144:145], v[216:217]
	s_and_b64 vcc, exec, s[8:9]
	v_mov_b64_e32 v[148:149], v[140:141]
	v_mov_b64_e32 v[152:153], v[144:145]
	v_mov_b64_e32 v[146:147], v[138:139]
	v_mov_b64_e32 v[150:151], v[142:143]
	s_cbranch_vccnz .LBB0_1100
	s_add_u32 s40, s61, s30
	s_addc_u32 s41, s62, s31
	v_lshl_add_u64 v[146:147], s[40:41], 0, v[180:181]
	v_lshl_add_u64 v[146:147], v[146:147], 0, s[20:21]
	v_lshl_add_u64 v[146:147], v[146:147], 0, v[170:171]
	global_load_dwordx4 v[150:153], v[146:147], off
	s_nop 0
	global_load_dwordx4 v[146:149], v[146:147], off offset:2048

; #define GAS __attribute__((address_space(1)))
;     __device__ __forceinline__ bool operator()(f32x4 (&acc)[2][2][4][2], const Unit& u, int wr, int wc, int fr, int fq, LAS unsigned char* scr) const {
;     ...
;             for (int m = 0; m < 4; ++m) { const size_t rg = (size_t)(rowb + ai * 128 + m * 16);
;                 const GAS bf16_t* gpa = H + HOFF(C_GA + colb, rg + lr) + lch * 8; const GAS bf16_t* gph = H + HOFF(C_GH + colb, rg + lr) + lch * 8;
;                 const u32x4 ga0 = *(const GAS u32x4*)gpa, ga1 = *(const GAS u32x4*)(gpa + 8 * 128);
;                 u32x4 gh0 = ga0, gh1 = ga1; if (seg0) { gh0 = *(const GAS u32x4*)gph; gh1 = *(const GAS u32x4*)(gph + 8 * 128); }
.LBB0_1110:
	s_add_i32 s38, s34, 0x90
	s_ashr_i32 s39, s38, 31
	v_lshl_add_u64 v[138:139], s[38:39], 0, v[160:161]
	v_lshlrev_b64 v[180:181], 8, v[138:139]
	v_lshl_add_u64 v[138:139], s[36:37], 0, v[180:181]
	v_lshl_add_u64 v[138:139], v[138:139], 0, s[20:21]
	v_mov_b32_e32 v171, v159
	v_lshl_add_u64 v[142:143], v[138:139], 0, v[170:171]
	v_mov_b64_e32 v[138:139], v[226:227]
	v_mov_b64_e32 v[140:141], v[228:229]
	s_nop 0
	v_mov_b64_e32 v[142:143], v[222:223]
	v_mov_b64_e32 v[144:145], v[224:225]
	s_and_b64 vcc, exec, s[8:9]
	v_mov_b64_e32 v[148:149], v[140:141]
	v_mov_b64_e32 v[152:153], v[144:145]
	v_mov_b64_e32 v[146:147], v[138:139]
	v_mov_b64_e32 v[150:151], v[142:143]
	s_cbranch_vccnz .LBB0_1112
	s_add_u32 s40, s61, s30
	s_addc_u32 s41, s62, s31
	v_lshl_add_u64 v[146:147], s[40:41], 0, v[180:181]
	v_lshl_add_u64 v[146:147], v[146:147], 0, s[20:21]
	v_lshl_add_u64 v[146:147], v[146:147], 0, v[170:171]
	global_load_dwordx4 v[150:153], v[146:147], off
	s_nop 0
	global_load_dwordx4 v[146:149], v[146:147], off offset:2048

; #define GAS __attribute__((address_space(1)))
;     __device__ __forceinline__ bool operator()(f32x4 (&acc)[2][2][4][2], const Unit& u, int wr, int wc, int fr, int fq, LAS unsigned char* scr) const {
;     ...
;             for (int m = 0; m < 4; ++m) { const size_t rg = (size_t)(rowb + ai * 128 + m * 16);
;                 const GAS bf16_t* gpa = H + HOFF(C_GA + colb, rg + lr) + lch * 8; const GAS bf16_t* gph = H + HOFF(C_GH + colb, rg + lr) + lch * 8;
;                 const u32x4 ga0 = *(const GAS u32x4*)gpa, ga1 = *(const GAS u32x4*)(gpa + 8 * 128);
;                 u32x4 gh0 = ga0, gh1 = ga1; if (seg0) { gh0 = *(const GAS u32x4*)gph; gh1 = *(const GAS u32x4*)(gph + 8 * 128); }
.LBB0_1122:
	s_add_i32 s38, s34, 0xa0
	s_ashr_i32 s39, s38, 31
	v_lshl_add_u64 v[138:139], s[38:39], 0, v[160:161]
	v_lshlrev_b64 v[180:181], 8, v[138:139]
	v_lshl_add_u64 v[138:139], s[36:37], 0, v[180:181]
	v_lshl_add_u64 v[138:139], v[138:139], 0, s[20:21]
	v_mov_b32_e32 v171, v159
	v_lshl_add_u64 v[142:143], v[138:139], 0, v[170:171]
	v_mov_b64_e32 v[138:139], v[234:235]
	v_mov_b64_e32 v[140:141], v[236:237]
	s_nop 0
	v_mov_b64_e32 v[142:143], v[230:231]
	v_mov_b64_e32 v[144:145], v[232:233]
	s_and_b64 vcc, exec, s[8:9]
	v_mov_b64_e32 v[148:149], v[140:141]
	v_mov_b64_e32 v[152:153], v[144:145]
	v_mov_b64_e32 v[146:147], v[138:139]
	v_mov_b64_e32 v[150:151], v[142:143]
	s_cbranch_vccnz .LBB0_1124
	s_add_u32 s40, s61, s30
	s_addc_u32 s41, s62, s31
	v_lshl_add_u64 v[146:147], s[40:41], 0, v[180:181]
	v_lshl_add_u64 v[146:147], v[146:147], 0, s[20:21]
	v_lshl_add_u64 v[146:147], v[146:147], 0, v[170:171]
	global_load_dwordx4 v[150:153], v[146:147], off
	s_nop 0
	global_load_dwordx4 v[146:149], v[146:147], off offset:2048

; #define GAS __attribute__((address_space(1)))
;     __device__ __forceinline__ bool operator()(f32x4 (&acc)[2][2][4][2], const Unit& u, int wr, int wc, int fr, int fq, LAS unsigned char* scr) const {
;     ...
;             for (int m = 0; m < 4; ++m) { const size_t rg = (size_t)(rowb + ai * 128 + m * 16);
;                 const GAS bf16_t* gpa = H + HOFF(C_GA + colb, rg + lr) + lch * 8; const GAS bf16_t* gph = H + HOFF(C_GH + colb, rg + lr) + lch * 8;
;                 const u32x4 ga0 = *(const GAS u32x4*)gpa, ga1 = *(const GAS u32x4*)(gpa + 8 * 128);
;                 u32x4 gh0 = ga0, gh1 = ga1; if (seg0) { gh0 = *(const GAS u32x4*)gph; gh1 = *(const GAS u32x4*)(gph + 8 * 128); }
.LBB0_1134:
	s_addk_i32 s34, 0xb0
	s_ashr_i32 s35, s34, 31
	v_lshl_add_u64 v[138:139], s[34:35], 0, v[160:161]
	v_lshlrev_b64 v[180:181], 8, v[138:139]
	v_lshl_add_u64 v[138:139], s[36:37], 0, v[180:181]
	v_lshl_add_u64 v[138:139], v[138:139], 0, s[20:21]
	v_mov_b32_e32 v171, v159
	v_lshl_add_u64 v[142:143], v[138:139], 0, v[170:171]
	v_mov_b64_e32 v[138:139], v[242:243]
	v_mov_b64_e32 v[140:141], v[244:245]
	s_nop 0
	v_mov_b64_e32 v[142:143], v[238:239]
	v_mov_b64_e32 v[144:145], v[240:241]
	s_and_b64 vcc, exec, s[8:9]
	v_mov_b64_e32 v[148:149], v[140:141]
	v_mov_b64_e32 v[152:153], v[144:145]
	v_mov_b64_e32 v[146:147], v[138:139]
	v_mov_b64_e32 v[150:151], v[142:143]
	s_cbranch_vccnz .LBB0_1136
	s_add_u32 s30, s61, s30
	s_addc_u32 s31, s62, s31
	v_lshl_add_u64 v[146:147], s[30:31], 0, v[180:181]
	v_lshl_add_u64 v[146:147], v[146:147], 0, s[20:21]
	v_lshl_add_u64 v[146:147], v[146:147], 0, v[170:171]
	global_load_dwordx4 v[150:153], v[146:147], off
	s_nop 0
	global_load_dwordx4 v[146:149], v[146:147], off offset:2048

; __global__ void __launch_bounds__(512, 2) kfwd(Args args) {
	.amdhsa_kernel _Z4kfwd4Args
		.amdhsa_group_segment_fixed_size 0
		.amdhsa_private_segment_fixed_size 0
		.amdhsa_kernarg_size 440
		.amdhsa_user_sgpr_count 2
		.amdhsa_user_sgpr_dispatch_ptr 0
		.amdhsa_user_sgpr_queue_ptr 0
		.amdhsa_user_sgpr_kernarg_segment_ptr 1
		.amdhsa_user_sgpr_dispatch_id 0
		.amdhsa_user_sgpr_kernarg_preload_length 0
		.amdhsa_user_sgpr_kernarg_preload_offset 0
		.amdhsa_user_sgpr_private_segment_size 0
		.amdhsa_uses_dynamic_stack 0
		.amdhsa_enable_private_segment 0
		.amdhsa_system_sgpr_workgroup_id_x 1
		.amdhsa_system_sgpr_workgroup_id_y 0
		.amdhsa_system_sgpr_workgroup_id_z 0
		.amdhsa_system_sgpr_workgroup_info 0
		.amdhsa_system_vgpr_workitem_id 0
		.amdhsa_next_free_vgpr 256
		.amdhsa_next_free_sgpr 102
		.amdhsa_accum_offset 256
		.amdhsa_reserve_vcc 1
		.amdhsa_float_round_mode_32 0
		.amdhsa_float_round_mode_16_64 0
		.amdhsa_float_denorm_mode_32 3
		.amdhsa_float_denorm_mode_16_64 3
		.amdhsa_dx10_clamp 1
		.amdhsa_ieee_mode 1
		.amdhsa_fp16_overflow 0
		.amdhsa_tg_split 0
		.amdhsa_exception_fp_ieee_invalid_op 0
		.amdhsa_exception_fp_denorm_src 0
		.amdhsa_exception_fp_ieee_div_zero 0
		.amdhsa_exception_fp_ieee_overflow 0
		.amdhsa_exception_fp_ieee_underflow 0
		.amdhsa_exception_fp_ieee_inexact 0
		.amdhsa_exception_int_div_zero 0
	.end_amdhsa_kernel

; __global__ void __launch_bounds__(512, 2) kfwd(Args args) {
amdhsa.kernels:
  - .agpr_count:     0
    .args:
      - .offset:         0
        .size:           184
        .value_kind:     by_value
      - .offset:         184
        .size:           4
        .value_kind:     hidden_block_count_x
      - .offset:         188
        .size:           4
        .value_kind:     hidden_block_count_y
      - .offset:         192
        .size:           4
        .value_kind:     hidden_block_count_z
      - .offset:         196
        .size:           2
        .value_kind:     hidden_group_size_x
      - .offset:         198
        .size:           2
        .value_kind:     hidden_group_size_y
      - .offset:         200
        .size:           2
        .value_kind:     hidden_group_size_z
      - .offset:         202
        .size:           2
        .value_kind:     hidden_remainder_x
      - .offset:         204
        .size:           2
        .value_kind:     hidden_remainder_y
      - .offset:         206
        .size:           2
        .value_kind:     hidden_remainder_z
      - .offset:         224
        .size:           8
        .value_kind:     hidden_global_offset_x
      - .offset:         232
        .size:           8
        .value_kind:     hidden_global_offset_y
      - .offset:         240
        .size:           8
        .value_kind:     hidden_global_offset_z
      - .offset:         248
        .size:           2
        .value_kind:     hidden_grid_dims
      - .offset:         304
        .size:           4
        .value_kind:     hidden_dynamic_lds_size
    .group_segment_fixed_size: 0
    .kernarg_segment_align: 8
    .kernarg_segment_size: 440
    .language:       OpenCL C
    .language_version:
      - 2
      - 0
    .max_flat_workgroup_size: 512
    .name:           _Z4kfwd4Args
    .private_segment_fixed_size: 0
    .sgpr_count:     108
    .sgpr_spill_count: 92
    .symbol:         _Z4kfwd4Args.kd
    .uniform_work_group_size: 1
    .uses_dynamic_stack: false
    .vgpr_count:     256
    .vgpr_spill_count: 0
    .wavefront_size: 64
